# NSA selection: query blocks with at most 16 candidate blocks (iq<16) skip the top-16 rank loops (mask is 0xffff for every token)
# speedup vs baseline: 1.0169x; 1.0042x over previous
; #define LAS __attribute__((address_space(3)))
; __device__ __forceinline__ int kperm(int key) { return (key & ~12) | ((key & 4) << 1) | ((key & 8) >> 1); }
; __device__ __forceinline__ void unit(LAS unsigned char* lds, const bf16* Z, const bf16* kct, const bf16* vct, bf16* OAp, int b, int g, int iq, const int tid_in) {
;     int tid = tid_in; asm volatile("" : "+v"(tid));
;     const int lane = tid & 63, r32 = lane & 31, hi = lane >> 5; const int w = __builtin_amdgcn_readfirstlane(tid >> 6);
;     const int j = w >> 1, hq = 4 * g + j, tl = 32 * (w & 1) + r32, t0 = 64 * iq, t = t0 + tl;
;     const size_t rowZ = (size_t)(b * T + t) * ZLD;
;     LAS bf16* KS = (LAS bf16*)(lds + L_KS); LAS bf16* VT = (LAS bf16*)(lds + L_VT); LAS bf16* KC = (LAS bf16*)(lds + L_KC); LAS bf16* VC = (LAS bf16*)(lds + L_VC);
;     LAS float* IA = (LAS float*)(lds + L_IA); LAS float* IB = (LAS float*)(lds + L_IB); LAS unsigned* MSK = (LAS unsigned*)(lds + L_MASK); LAS int* TL = (LAS int*)(lds + L_TL);
;     bf16x8 qr[4];
; #pragma unroll
;     for (int d0 = 0; d0 < 4; ++d0) qr[d0] = *(const bf16x8*)(Z + rowZ + ZQ + hq * 64 + 16 * d0 + 8 * hi);
;     const float slope2 = __builtin_amdgcn_exp2f(-0.5f * (float)(hq + 1)) * LOG2E;
;     float gate[3];
; #pragma unroll
;     for (int x = 0; x < 3; ++x) gate[x] = sigmoidf_(bf2f(Z[rowZ + ZNG + hq * 3 + x]));
;     f32x16 otot[2];
; #pragma unroll
;     for (int r = 0; r < 16; ++r) { otot[0][r] = 0.f; otot[1][r] = 0.f; }
;     {
;         const bf16* kc = kct + (size_t)((b * 4 + g) * 128) * 64; const bf16* vc = vct + (size_t)((b * 4 + g) * 128) * 64;
; #pragma unroll
;         for (int q = 0; q < 2; ++q) { const int idx = tid + 512 * q, key = idx >> 3, ch = idx & 7;
;             const v4u kv = *(const v4u*)(kc + key * 64 + ch * 8); *(LAS v4u*)(KC + key * KST + ch * 8) = kv;
;             const v4u vv = *(const v4u*)(vc + key * 64 + ch * 8); const int pos = kperm(key);
;             const unsigned ww[4] = {vv.x, vv.y, vv.z, vv.w};
; #pragma unroll
;             for (int e = 0; e < 4; ++e) { VC[(ch * 8 + 2 * e) * VST2 + pos] = (bf16)(ww[e] & 0xffffu); VC[(ch * 8 + 2 * e + 1) * VST2 + pos] = (bf16)(ww[e] >> 16); } }
;     }
;     __syncthreads();
;     {
;         f32x16 p[4];
; #pragma unroll
;         for (int blk = 0; blk < 4; ++blk) {
; #pragma unroll
;             for (int r = 0; r < 16; ++r) p[blk][r] = 0.f;
; #pragma unroll
.LBB0_416:
	v_mov_b32_e32 v78, v123
	s_and_b32 s23, s4, 3
	s_ashr_i32 s5, s4, 2
	v_readfirstlane_b32 s0, v78
	v_and_b32_e32 v73, 31, v78
	s_ashr_i32 s4, s0, 7
	s_lshl_b32 s1, s23, 2
	s_lshr_b32 s0, s0, 1
	s_add_i32 s6, s4, s1
	v_and_or_b32 v68, s0, 32, v73
	v_readlane_b32 s0, v253, 32
	v_lshl_or_b32 v77, s18, 6, v68
	s_lshl_b32 s22, s5, 11
	v_readlane_b32 s1, v253, 33
	v_or_b32_e32 v118, s22, v77
	s_lshl_b32 s16, s6, 6
	v_mov_b64_e32 v[2:3], s[0:1]
	v_mad_i64_i32 v[2:3], s[0:1], v118, s26, v[2:3]
	s_add_i32 s0, s6, 1
	v_bfe_u32 v74, v78, 5, 1
	s_ashr_i32 s17, s16, 31
	v_cvt_f32_i32_e32 v1, s0
	s_mul_i32 s0, s6, 3
	v_lshl_add_u64 v[4:5], s[16:17], 1, v[2:3]
	v_lshlrev_b32_e32 v120, 4, v74
	v_mov_b32_e32 v121, v187
	s_ashr_i32 s1, s0, 31
	v_lshl_add_u64 v[4:5], v[4:5], 0, v[120:121]
	v_lshl_add_u64 v[2:3], s[0:1], 1, v[2:3]
	s_mov_b64 s[0:1], 0x1400
	global_load_dwordx4 v[98:101], v[4:5], off
	global_load_dwordx4 v[102:105], v[4:5], off offset:32
	global_load_dwordx4 v[106:109], v[4:5], off offset:64
	global_load_dwordx4 v[110:113], v[4:5], off offset:96
	v_lshl_add_u64 v[4:5], v[2:3], 0, s[0:1]
	s_lshl_b32 s0, s5, 9
	s_lshl_b32 s28, s23, 7
	v_add_co_u32_e32 v2, vcc, s97, v2
	s_or_b32 s0, s28, s0
	s_nop 0
	v_addc_co_u32_e32 v3, vcc, 0, v3, vcc
	s_ashr_i32 s1, s0, 31
	global_load_dword v69, v[2:3], off offset:1024
	global_load_ushort v121, v[4:5], off offset:4
	s_lshl_b64 s[0:1], s[0:1], 7
	v_readlane_b32 s5, v252, 0
	v_lshlrev_b32_e32 v2, 3, v78
	v_ashrrev_i32_e32 v119, 3, v78
	s_add_u32 s6, s5, s0
	v_readlane_b32 s5, v252, 1
	v_and_b32_e32 v9, 56, v2
	v_lshlrev_b32_e32 v2, 6, v119
	s_addc_u32 s7, s5, s1
	v_lshlrev_b32_e32 v186, 1, v9
	v_ashrrev_i32_e32 v3, 31, v2
	v_lshl_add_u64 v[6:7], s[6:7], 0, v[186:187]
	v_lshlrev_b64 v[12:13], 1, v[2:3]
	v_lshl_add_u64 v[2:3], v[6:7], 0, v[12:13]
	global_load_dwordx4 v[200:203], v[2:3], off
	v_readlane_b32 s5, v252, 4
	s_add_u32 s0, s5, s0
	v_readlane_b32 s5, v252, 5
	s_addc_u32 s1, s5, s1
	v_add_u32_e32 v8, 0, v186
	s_movk_i32 s5, 0x90
	v_lshl_add_u64 v[10:11], s[0:1], 0, v[186:187]
	v_mad_u64_u32 v[14:15], s[0:1], v119, s5, v[8:9]
	s_movk_i32 s0, 0x10e
	s_nop 0
	v_mad_u32_u24 v9, v9, s0, v8
	v_lshl_add_u64 v[2:3], v[10:11], 0, v[12:13]
	global_load_dwordx4 v[204:207], v[2:3], off
	v_add_u32_e32 v2, 0x200, v78
	v_ashrrev_i32_e32 v15, 3, v2
	v_lshlrev_b32_e32 v2, 6, v15
	v_ashrrev_i32_e32 v3, 31, v2
	v_lshlrev_b64 v[2:3], 1, v[2:3]
	v_lshl_add_u64 v[4:5], v[6:7], 0, v[2:3]
	global_load_dwordx4 v[208:211], v[4:5], off
	v_lshl_add_u64 v[4:5], v[10:11], 0, v[2:3]
	global_load_dwordx4 v[212:215], v[4:5], off
	v_add_u32_e32 v76, 0, v120
	v_mad_u32_u24 v66, v73, s5, v76
	v_mul_f32_e32 v1, -0.5, v1
	v_exp_f32_e32 v1, v1
	v_lshlrev_b32_e32 v122, 2, v74
	v_and_b32_e32 v79, 63, v78
	v_cmp_eq_u32_e64 s[44:45], 0, v73
	v_mul_f32_e32 v124, 0x3fb8aa3b, v1
	v_lshlrev_b32_e32 v5, 1, v119
	v_lshrrev_b32_e32 v12, 1, v119
	v_and_b32_e32 v4, 0x7ffffff3, v119
	v_and_b32_e32 v5, 8, v5
	v_and_b32_e32 v12, 4, v12
	v_or3_b32 v4, v5, v4, v12
	v_lshl_add_u32 v12, v4, 1, v9
	v_mad_u64_u32 v[6:7], s[0:1], v15, s5, v[8:9]
	v_lshlrev_b32_e32 v5, 1, v15
	v_lshrrev_b32_e32 v13, 1, v15
	v_and_b32_e32 v4, 0x7ffffff3, v15
	v_and_b32_e32 v5, 8, v5
	v_and_b32_e32 v13, 4, v13
	v_or3_b32 v4, v5, v4, v13
	v_lshl_add_u32 v13, v4, 1, v9
	s_mov_b32 s5, 0xff800000
	v_cmp_gt_u32_e64 s[0:1], 32, v79
	s_waitcnt vmcnt(3)
	ds_write_b128 v14, v[200:203] offset:18432
	s_waitcnt vmcnt(2)
	ds_write_b16 v12, v204 offset:36864
	ds_write_b16_d16_hi v12, v204 offset:37136
	ds_write_b16 v12, v205 offset:37408
	ds_write_b16_d16_hi v12, v205 offset:37680
	ds_write_b16 v12, v206 offset:37952
	ds_write_b16_d16_hi v12, v206 offset:38224
	ds_write_b16 v12, v207 offset:38496
	ds_write_b16_d16_hi v12, v207 offset:38768
	s_waitcnt vmcnt(1)
	ds_write_b128 v6, v[208:211] offset:18432
	s_waitcnt vmcnt(0)
	ds_write_b16 v13, v212 offset:36864
	ds_write_b16_d16_hi v13, v212 offset:37136
	ds_write_b16 v13, v213 offset:37408
	ds_write_b16_d16_hi v13, v213 offset:37680
	ds_write_b16 v13, v214 offset:37952
	ds_write_b16_d16_hi v13, v214 offset:38224
	ds_write_b16 v13, v215 offset:38496
	ds_write_b16_d16_hi v13, v215 offset:38768
	s_waitcnt lgkmcnt(0)
	s_barrier
	ds_read_b128 v[2:5], v66 offset:18432
	ds_read_b128 v[6:9], v66 offset:18464
	s_waitcnt lgkmcnt(1)
	v_mfma_f32_32x32x16_bf16 v[50:65], v[2:5], v[98:101], 0
	ds_read_b128 v[2:5], v66 offset:18496
	ds_read_b128 v[80:83], v66 offset:32288
	s_waitcnt lgkmcnt(2)
	v_mfma_f32_32x32x16_bf16 v[50:65], v[6:9], v[102:105], v[50:65]
	s_waitcnt lgkmcnt(1)
	v_mfma_f32_32x32x16_bf16 v[50:65], v[2:5], v[106:109], v[50:65]
	ds_read_b128 v[2:5], v66 offset:18528
	s_waitcnt lgkmcnt(0)
	v_mfma_f32_32x32x16_bf16 v[50:65], v[2:5], v[110:113], v[50:65]
	ds_read_b128 v[2:5], v66 offset:23040
	s_waitcnt lgkmcnt(0)
	v_mfma_f32_32x32x16_bf16 v[34:49], v[2:5], v[98:101], 0
	ds_read_b128 v[2:5], v66 offset:23072
	s_waitcnt lgkmcnt(0)
	v_mfma_f32_32x32x16_bf16 v[34:49], v[2:5], v[102:105], v[34:49]
	ds_read_b128 v[2:5], v66 offset:23104
	s_waitcnt lgkmcnt(0)
	v_mfma_f32_32x32x16_bf16 v[34:49], v[2:5], v[106:109], v[34:49]
	ds_read_b128 v[2:5], v66 offset:23136
	s_waitcnt lgkmcnt(0)
	v_mfma_f32_32x32x16_bf16 v[34:49], v[2:5], v[110:113], v[34:49]
	ds_read_b128 v[2:5], v66 offset:27648
	s_waitcnt lgkmcnt(0)
	v_mfma_f32_32x32x16_bf16 v[18:33], v[2:5], v[98:101], 0
	ds_read_b128 v[2:5], v66 offset:27680
	s_waitcnt lgkmcnt(0)
	v_mfma_f32_32x32x16_bf16 v[18:33], v[2:5], v[102:105], v[18:33]
	ds_read_b128 v[2:5], v66 offset:27712
	s_waitcnt lgkmcnt(0)
	v_mfma_f32_32x32x16_bf16 v[18:33], v[2:5], v[106:109], v[18:33]
	ds_read_b128 v[2:5], v66 offset:27744
	s_waitcnt lgkmcnt(0)
; #define LAS __attribute__((address_space(3)))
; __device__ __forceinline__ int crow(int r, int hi) { return (r & 3) + 8 * (r >> 2) + 4 * hi; }
; #define MFMA32(a, b, c) __builtin_amdgcn_mfma_f32_32x32x16_bf16((a), (b), (c), 0, 0, 0)
; __device__ __forceinline__ void unit(LAS unsigned char* lds, const bf16* Z, const bf16* kct, const bf16* vct, bf16* OAp, int b, int g, int iq, const int tid_in) {
;     ...
;             for (int d0 = 0; d0 < 4; ++d0) { const bf16x8 kf = *(const LAS bf16x8*)(KC + (32 * blk + r32) * KST + 16 * d0 + 8 * hi); p[blk] = MFMA32(kf, qr[d0], p[blk]); }
;         }
;         float mx = -INFINITY;
; #pragma unroll
;         for (int blk = 0; blk < 4; ++blk)
; #pragma unroll
;             for (int r = 0; r < 16; ++r) { const int c = 32 * blk + crow(r, hi); const int dist = t - (16 * c + 31); const bool ok = (dist >= 0) && (c < 127);
;                 const float s = ok ? p[blk][r] - slope2 * (float)dist : -INFINITY; p[blk][r] = s; mx = fmaxf(mx, s); }
	v_mfma_f32_32x32x16_bf16 v[18:33], v[2:5], v[110:113], v[18:33]
	ds_read_b128 v[2:5], v66 offset:32256
	s_waitcnt lgkmcnt(0)
	v_mfma_f32_32x32x16_bf16 v[2:17], v[2:5], v[98:101], 0
	v_mfma_f32_32x32x16_bf16 v[2:17], v[80:83], v[102:105], v[2:17]
	ds_read_b128 v[80:83], v66 offset:32320
	s_waitcnt lgkmcnt(0)
	v_mfma_f32_32x32x16_bf16 v[2:17], v[80:83], v[106:109], v[2:17]
	ds_read_b128 v[80:83], v66 offset:32352
	s_waitcnt lgkmcnt(0)
	v_mfma_f32_32x32x16_bf16 v[2:17], v[80:83], v[110:113], v[2:17]
	v_subrev_u32_e32 v80, 31, v77
	v_lshlrev_b32_e32 v81, 6, v74
	v_sub_u32_e32 v1, v80, v81
	v_cmp_lt_i32_e32 vcc, -1, v1
	v_cvt_f32_u32_e32 v1, v1
	v_fma_f32 v1, -v124, v1, v50
	v_cndmask_b32_e32 v66, v229, v1, vcc
	v_or_b32_e32 v1, 16, v81
	v_sub_u32_e32 v1, v80, v1
	v_cmp_lt_i32_e32 vcc, -1, v1
	v_cvt_f32_u32_e32 v1, v1
	v_or_b32_e32 v50, 2, v122
	v_lshlrev_b32_e32 v71, 4, v50
	v_sub_u32_e32 v71, v80, v71
	v_fma_f32 v1, -v124, v1, v51
	v_cndmask_b32_e32 v67, v229, v1, vcc
	v_cmp_lt_i32_e32 vcc, -1, v71
	v_cvt_f32_u32_e32 v71, v71
	v_or_b32_e32 v1, 3, v122
	v_max3_f32 v70, v66, s5, v67
	v_mov_b32_e32 v51, v122
	v_fma_f32 v52, -v124, v71, v52
	v_lshlrev_b32_e32 v71, 4, v1
	v_sub_u32_e32 v71, v80, v71
	v_cndmask_b32_e32 v52, v229, v52, vcc
	v_cmp_lt_i32_e32 vcc, -1, v71
	v_cvt_f32_u32_e32 v71, v71
	v_fma_f32 v53, -v124, v71, v53
	v_cndmask_b32_e32 v53, v229, v53, vcc
	v_max3_f32 v71, v70, v52, v53
	v_or_b32_e32 v70, 8, v122
	v_lshlrev_b32_e32 v72, 4, v70
	v_sub_u32_e32 v72, v80, v72
	v_cmp_lt_i32_e32 vcc, -1, v72
	v_cvt_f32_u32_e32 v72, v72
	v_fma_f32 v54, -v124, v72, v54
	v_or_b32_e32 v72, 0x90, v81
	v_sub_u32_e32 v72, v80, v72
	v_cndmask_b32_e32 v54, v229, v54, vcc
	v_cmp_lt_i32_e32 vcc, -1, v72
	v_cvt_f32_u32_e32 v72, v72
	v_fma_f32 v55, -v124, v72, v55
	v_or_b32_e32 v72, 0xa0, v81
	v_sub_u32_e32 v72, v80, v72
	v_cndmask_b32_e32 v55, v229, v55, vcc
	v_cmp_lt_i32_e32 vcc, -1, v72
	v_cvt_f32_u32_e32 v72, v72
	v_max3_f32 v71, v71, v54, v55
	v_fma_f32 v56, -v124, v72, v56
	v_or_b32_e32 v72, 0xb0, v81
	v_sub_u32_e32 v72, v80, v72
	v_cndmask_b32_e32 v56, v229, v56, vcc
	v_cmp_lt_i32_e32 vcc, -1, v72
	v_cvt_f32_u32_e32 v72, v72
	v_fma_f32 v57, -v124, v72, v57
	v_cndmask_b32_e32 v57, v229, v57, vcc
	v_max3_f32 v72, v71, v56, v57
	v_or_b32_e32 v71, 16, v122
	v_lshlrev_b32_e32 v75, 4, v71
	v_sub_u32_e32 v75, v80, v75
	v_cmp_lt_i32_e32 vcc, -1, v75
	v_cvt_f32_u32_e32 v75, v75
	v_fma_f32 v58, -v124, v75, v58
	v_or_b32_e32 v75, 0x110, v81
	v_sub_u32_e32 v75, v80, v75
	v_cndmask_b32_e32 v58, v229, v58, vcc
	v_cmp_lt_i32_e32 vcc, -1, v75
	v_cvt_f32_u32_e32 v75, v75
	v_fma_f32 v59, -v124, v75, v59
	v_or_b32_e32 v75, 0x120, v81
	v_sub_u32_e32 v75, v80, v75
	v_cndmask_b32_e32 v59, v229, v59, vcc
	v_cmp_lt_i32_e32 vcc, -1, v75
	v_cvt_f32_u32_e32 v75, v75
	v_max3_f32 v72, v72, v58, v59
	v_fma_f32 v60, -v124, v75, v60
	v_or_b32_e32 v75, 0x130, v81
	v_sub_u32_e32 v75, v80, v75
	v_cndmask_b32_e32 v60, v229, v60, vcc
	v_cmp_lt_i32_e32 vcc, -1, v75
	v_cvt_f32_u32_e32 v75, v75
	v_fma_f32 v61, -v124, v75, v61
	v_cndmask_b32_e32 v61, v229, v61, vcc
	v_max3_f32 v75, v72, v60, v61
	v_or_b32_e32 v72, 24, v122
	v_lshlrev_b32_e32 v82, 4, v72
	v_sub_u32_e32 v82, v80, v82
	v_cmp_lt_i32_e32 vcc, -1, v82
	v_cvt_f32_u32_e32 v82, v82
	v_fma_f32 v62, -v124, v82, v62
	v_or_b32_e32 v82, 0x190, v81
	v_sub_u32_e32 v82, v80, v82
	v_cndmask_b32_e32 v62, v229, v62, vcc
	v_cmp_lt_i32_e32 vcc, -1, v82
	v_cvt_f32_u32_e32 v82, v82
	v_fma_f32 v63, -v124, v82, v63
	v_or_b32_e32 v82, 0x1a0, v81
	v_sub_u32_e32 v82, v80, v82
	v_cndmask_b32_e32 v63, v229, v63, vcc
	v_cmp_lt_i32_e32 vcc, -1, v82
	v_cvt_f32_u32_e32 v82, v82
	v_max3_f32 v75, v75, v62, v63
	v_fma_f32 v64, -v124, v82, v64
	v_or_b32_e32 v82, 0x1b0, v81
	v_sub_u32_e32 v82, v80, v82
	v_cndmask_b32_e32 v64, v229, v64, vcc
	v_cmp_lt_i32_e32 vcc, -1, v82
	v_cvt_f32_u32_e32 v82, v82
	v_fma_f32 v65, -v124, v82, v65
	v_cndmask_b32_e32 v65, v229, v65, vcc
	v_max3_f32 v82, v75, v64, v65
	v_or_b32_e32 v75, 32, v122
	v_lshlrev_b32_e32 v83, 4, v75
	v_sub_u32_e32 v83, v80, v83
	v_cmp_lt_i32_e32 vcc, -1, v83
	v_cvt_f32_u32_e32 v83, v83
	v_fma_f32 v34, -v124, v83, v34
	v_or_b32_e32 v83, 0x210, v81
	v_sub_u32_e32 v83, v80, v83
	v_cndmask_b32_e32 v34, v229, v34, vcc
	v_cmp_lt_i32_e32 vcc, -1, v83
	v_cvt_f32_u32_e32 v83, v83
	v_fma_f32 v35, -v124, v83, v35
	v_or_b32_e32 v83, 0x220, v81
	v_sub_u32_e32 v83, v80, v83
	v_cndmask_b32_e32 v35, v229, v35, vcc
	v_cmp_lt_i32_e32 vcc, -1, v83
	v_cvt_f32_u32_e32 v83, v83
	v_max3_f32 v82, v82, v34, v35
	v_fma_f32 v36, -v124, v83, v36
	v_or_b32_e32 v83, 0x230, v81
	v_sub_u32_e32 v83, v80, v83
	v_cndmask_b32_e32 v36, v229, v36, vcc
	v_cmp_lt_i32_e32 vcc, -1, v83
	v_cvt_f32_u32_e32 v83, v83
	v_fma_f32 v37, -v124, v83, v37
	v_or_b32_e32 v83, 0x280, v81
	v_sub_u32_e32 v83, v80, v83
	v_cndmask_b32_e32 v37, v229, v37, vcc
	v_cmp_lt_i32_e32 vcc, -1, v83
	v_cvt_f32_u32_e32 v83, v83
	v_max3_f32 v82, v82, v36, v37
	v_fma_f32 v38, -v124, v83, v38
	v_or_b32_e32 v83, 0x290, v81
	v_sub_u32_e32 v83, v80, v83
	v_cndmask_b32_e32 v38, v229, v38, vcc
	v_cmp_lt_i32_e32 vcc, -1, v83
	v_cvt_f32_u32_e32 v83, v83
	v_fma_f32 v39, -v124, v83, v39
	v_or_b32_e32 v83, 0x2a0, v81
	v_sub_u32_e32 v83, v80, v83
	v_cndmask_b32_e32 v39, v229, v39, vcc
	v_cmp_lt_i32_e32 vcc, -1, v83
	v_cvt_f32_u32_e32 v83, v83
	v_max3_f32 v82, v82, v38, v39
	v_fma_f32 v40, -v124, v83, v40
	v_or_b32_e32 v83, 0x2b0, v81
	v_sub_u32_e32 v83, v80, v83
	v_cndmask_b32_e32 v40, v229, v40, vcc
	v_cmp_lt_i32_e32 vcc, -1, v83
	v_cvt_f32_u32_e32 v83, v83
	v_fma_f32 v41, -v124, v83, v41
	v_or_b32_e32 v83, 0x300, v81
	v_sub_u32_e32 v83, v80, v83
	v_cndmask_b32_e32 v41, v229, v41, vcc
; __device__ __forceinline__ int crow(int r, int hi) { return (r & 3) + 8 * (r >> 2) + 4 * hi; }
; __device__ __forceinline__ void unit(LAS unsigned char* lds, const bf16* Z, const bf16* kct, const bf16* vct, bf16* OAp, int b, int g, int iq, const int tid_in) {
;     ...
;             for (int r = 0; r < 16; ++r) { const int c = 32 * blk + crow(r, hi); const int dist = t - (16 * c + 31); const bool ok = (dist >= 0) && (c < 127);
;                 const float s = ok ? p[blk][r] - slope2 * (float)dist : -INFINITY; p[blk][r] = s; mx = fmaxf(mx, s); }
	v_cmp_lt_i32_e32 vcc, -1, v83
	v_cvt_f32_u32_e32 v83, v83
	v_max3_f32 v82, v82, v40, v41
	v_fma_f32 v42, -v124, v83, v42
	v_or_b32_e32 v83, 0x310, v81
	v_sub_u32_e32 v83, v80, v83
	v_cndmask_b32_e32 v42, v229, v42, vcc
	v_cmp_lt_i32_e32 vcc, -1, v83
	v_cvt_f32_u32_e32 v83, v83
	v_fma_f32 v43, -v124, v83, v43
	v_or_b32_e32 v83, 0x320, v81
	v_sub_u32_e32 v83, v80, v83
	v_cndmask_b32_e32 v43, v229, v43, vcc
	v_cmp_lt_i32_e32 vcc, -1, v83
	v_cvt_f32_u32_e32 v83, v83
	v_max3_f32 v82, v82, v42, v43
	v_fma_f32 v44, -v124, v83, v44
	v_or_b32_e32 v83, 0x330, v81
	v_sub_u32_e32 v83, v80, v83
	v_cndmask_b32_e32 v44, v229, v44, vcc
	v_cmp_lt_i32_e32 vcc, -1, v83
	v_cvt_f32_u32_e32 v83, v83
	v_fma_f32 v45, -v124, v83, v45
	v_or_b32_e32 v83, 0x380, v81
	v_sub_u32_e32 v83, v80, v83
	v_cndmask_b32_e32 v45, v229, v45, vcc
	v_cmp_lt_i32_e32 vcc, -1, v83
	v_cvt_f32_u32_e32 v83, v83
	v_max3_f32 v82, v82, v44, v45
	v_fma_f32 v46, -v124, v83, v46
	v_or_b32_e32 v83, 0x390, v81
	v_sub_u32_e32 v83, v80, v83
	v_cndmask_b32_e32 v46, v229, v46, vcc
	v_cmp_lt_i32_e32 vcc, -1, v83
	v_cvt_f32_u32_e32 v83, v83
	v_fma_f32 v47, -v124, v83, v47
	v_or_b32_e32 v83, 0x3a0, v81
	v_sub_u32_e32 v83, v80, v83
	v_cndmask_b32_e32 v47, v229, v47, vcc
	v_cmp_lt_i32_e32 vcc, -1, v83
	v_cvt_f32_u32_e32 v83, v83
	v_max3_f32 v82, v82, v46, v47
	v_fma_f32 v48, -v124, v83, v48
	v_or_b32_e32 v83, 0x3b0, v81
	v_sub_u32_e32 v83, v80, v83
	v_cndmask_b32_e32 v48, v229, v48, vcc
	v_cmp_lt_i32_e32 vcc, -1, v83
	v_cvt_f32_u32_e32 v83, v83
	v_fma_f32 v49, -v124, v83, v49
	v_cndmask_b32_e32 v49, v229, v49, vcc
	v_max3_f32 v84, v82, v48, v49
	v_or_b32_e32 v82, 0x400, v81
	v_sub_u32_e32 v82, v80, v82
	v_cmp_lt_i32_e32 vcc, -1, v82
	v_cvt_f32_u32_e32 v82, v82
	v_fma_f32 v18, -v124, v82, v18
	v_cndmask_b32_e32 v82, v229, v18, vcc
	v_or_b32_e32 v18, 0x410, v81
	v_sub_u32_e32 v18, v80, v18
	v_cmp_lt_i32_e32 vcc, -1, v18
	v_cvt_f32_u32_e32 v18, v18
	v_fma_f32 v18, -v124, v18, v19
	v_or_b32_e32 v19, 0x420, v81
	v_sub_u32_e32 v19, v80, v19
	v_cndmask_b32_e32 v83, v229, v18, vcc
	v_cmp_lt_i32_e32 vcc, -1, v19
	v_cvt_f32_u32_e32 v19, v19
	v_max3_f32 v18, v84, v82, v83
	v_fma_f32 v19, -v124, v19, v20
	v_cndmask_b32_e32 v84, v229, v19, vcc
	v_or_b32_e32 v19, 0x430, v81
	v_sub_u32_e32 v19, v80, v19
	v_cmp_lt_i32_e32 vcc, -1, v19
	v_cvt_f32_u32_e32 v19, v19
	v_fma_f32 v19, -v124, v19, v21
	v_cndmask_b32_e32 v85, v229, v19, vcc
	v_or_b32_e32 v19, 0x480, v81
	v_sub_u32_e32 v19, v80, v19
	v_cmp_lt_i32_e32 vcc, -1, v19
	v_cvt_f32_u32_e32 v19, v19
	v_max3_f32 v18, v18, v84, v85
	v_fma_f32 v19, -v124, v19, v22
	v_cndmask_b32_e32 v86, v229, v19, vcc
	v_or_b32_e32 v19, 0x490, v81
	v_sub_u32_e32 v19, v80, v19
	v_cmp_lt_i32_e32 vcc, -1, v19
	v_cvt_f32_u32_e32 v19, v19
	v_fma_f32 v19, -v124, v19, v23
	v_cndmask_b32_e32 v87, v229, v19, vcc
	v_or_b32_e32 v19, 0x4a0, v81
	v_sub_u32_e32 v19, v80, v19
	v_cmp_lt_i32_e32 vcc, -1, v19
	v_cvt_f32_u32_e32 v19, v19
	v_max3_f32 v18, v18, v86, v87
	v_fma_f32 v19, -v124, v19, v24
	v_cndmask_b32_e32 v24, v229, v19, vcc
	v_or_b32_e32 v19, 0x4b0, v81
	v_sub_u32_e32 v19, v80, v19
	v_cmp_lt_i32_e32 vcc, -1, v19
	v_cvt_f32_u32_e32 v19, v19
	v_fma_f32 v19, -v124, v19, v25
	v_cndmask_b32_e32 v25, v229, v19, vcc
	v_or_b32_e32 v19, 0x500, v81
	v_sub_u32_e32 v19, v80, v19
	v_cmp_lt_i32_e32 vcc, -1, v19
	v_cvt_f32_u32_e32 v19, v19
	v_max3_f32 v18, v18, v24, v25
	v_fma_f32 v19, -v124, v19, v26
	v_cndmask_b32_e32 v26, v229, v19, vcc
	v_or_b32_e32 v19, 0x510, v81
	v_sub_u32_e32 v19, v80, v19
	v_cmp_lt_i32_e32 vcc, -1, v19
	v_cvt_f32_u32_e32 v19, v19
	v_fma_f32 v19, -v124, v19, v27
	v_cndmask_b32_e32 v27, v229, v19, vcc
	v_or_b32_e32 v19, 0x520, v81
	v_sub_u32_e32 v19, v80, v19
	v_cmp_lt_i32_e32 vcc, -1, v19
	v_cvt_f32_u32_e32 v19, v19
	v_max3_f32 v18, v18, v26, v27
	v_fma_f32 v19, -v124, v19, v28
	v_cndmask_b32_e32 v28, v229, v19, vcc
	v_or_b32_e32 v19, 0x530, v81
	v_sub_u32_e32 v19, v80, v19
	v_cmp_lt_i32_e32 vcc, -1, v19
	v_cvt_f32_u32_e32 v19, v19
	v_fma_f32 v19, -v124, v19, v29
	v_cndmask_b32_e32 v29, v229, v19, vcc
	v_or_b32_e32 v19, 0x580, v81
	v_sub_u32_e32 v19, v80, v19
	v_cmp_lt_i32_e32 vcc, -1, v19
	v_cvt_f32_u32_e32 v19, v19
	v_max3_f32 v18, v18, v28, v29
	v_fma_f32 v19, -v124, v19, v30
	v_cndmask_b32_e32 v30, v229, v19, vcc
	v_or_b32_e32 v19, 0x590, v81
	v_sub_u32_e32 v19, v80, v19
	v_cmp_lt_i32_e32 vcc, -1, v19
	v_cvt_f32_u32_e32 v19, v19
	v_fma_f32 v19, -v124, v19, v31
	v_cndmask_b32_e32 v31, v229, v19, vcc
	v_or_b32_e32 v19, 0x5a0, v81
	v_sub_u32_e32 v19, v80, v19
	v_cmp_lt_i32_e32 vcc, -1, v19
	v_cvt_f32_u32_e32 v19, v19
	v_max3_f32 v18, v18, v30, v31
	v_fma_f32 v19, -v124, v19, v32
	v_cndmask_b32_e32 v32, v229, v19, vcc
	v_or_b32_e32 v19, 0x5b0, v81
	v_sub_u32_e32 v19, v80, v19
	v_cmp_lt_i32_e32 vcc, -1, v19
	v_cvt_f32_u32_e32 v19, v19
	v_fma_f32 v19, -v124, v19, v33
	v_cndmask_b32_e32 v33, v229, v19, vcc
	v_or_b32_e32 v19, 0x600, v81
	v_sub_u32_e32 v19, v80, v19
	v_cmp_lt_i32_e32 vcc, -1, v19
	v_cvt_f32_u32_e32 v19, v19
	v_max3_f32 v18, v18, v32, v33
	v_fma_f32 v2, -v124, v19, v2
	v_cndmask_b32_e32 v88, v229, v2, vcc
	v_or_b32_e32 v2, 0x610, v81
	v_sub_u32_e32 v2, v80, v2
	v_cmp_lt_i32_e32 vcc, -1, v2
	v_cvt_f32_u32_e32 v2, v2
	v_fma_f32 v2, -v124, v2, v3
	v_or_b32_e32 v3, 0x620, v81
	v_sub_u32_e32 v3, v80, v3
	v_cndmask_b32_e32 v89, v229, v2, vcc
	v_cmp_lt_i32_e32 vcc, -1, v3
	v_cvt_f32_u32_e32 v3, v3
	v_max3_f32 v2, v18, v88, v89
	v_fma_f32 v3, -v124, v3, v4
	v_cndmask_b32_e32 v90, v229, v3, vcc
	v_or_b32_e32 v3, 0x630, v81
	v_sub_u32_e32 v3, v80, v3
	v_cmp_lt_i32_e32 vcc, -1, v3
	v_cvt_f32_u32_e32 v3, v3
	v_and_b32_e32 v4, 64, v228
	v_fma_f32 v3, -v124, v3, v5
; __device__ __forceinline__ int crow(int r, int hi) { return (r & 3) + 8 * (r >> 2) + 4 * hi; }
; __device__ __forceinline__ void unit(LAS unsigned char* lds, const bf16* Z, const bf16* kct, const bf16* vct, bf16* OAp, int b, int g, int iq, const int tid_in) {
;     ...
;             for (int r = 0; r < 16; ++r) { const int c = 32 * blk + crow(r, hi); const int dist = t - (16 * c + 31); const bool ok = (dist >= 0) && (c < 127);
;                 const float s = ok ? p[blk][r] - slope2 * (float)dist : -INFINITY; p[blk][r] = s; mx = fmaxf(mx, s); }
;         mx = fmaxf(mx, __shfl_xor(mx, 32));
;         const float msafe = (mx == -INFINITY) ? 0.f : mx;
;         float l = 0.f;
; #pragma unroll
;         for (int blk = 0; blk < 4; ++blk)
; #pragma unroll
;             for (int r = 0; r < 16; ++r) { const float e = __builtin_amdgcn_exp2f(p[blk][r] - msafe); p[blk][r] = e; l += e; }
	v_cndmask_b32_e32 v91, v229, v3, vcc
	v_or_b32_e32 v3, 0x680, v81
	v_sub_u32_e32 v3, v80, v3
	v_cmp_lt_i32_e32 vcc, -1, v3
	v_cvt_f32_u32_e32 v3, v3
	v_max3_f32 v2, v2, v90, v91
	v_fma_f32 v3, -v124, v3, v6
	v_cndmask_b32_e32 v92, v229, v3, vcc
	v_or_b32_e32 v3, 0x690, v81
	v_sub_u32_e32 v3, v80, v3
	v_cmp_lt_i32_e32 vcc, -1, v3
	v_cvt_f32_u32_e32 v3, v3
	v_fma_f32 v3, -v124, v3, v7
	v_cndmask_b32_e32 v93, v229, v3, vcc
	v_or_b32_e32 v3, 0x6a0, v81
	v_sub_u32_e32 v3, v80, v3
	v_cmp_lt_i32_e32 vcc, -1, v3
	v_cvt_f32_u32_e32 v3, v3
	v_max3_f32 v2, v2, v92, v93
	v_fma_f32 v3, -v124, v3, v8
	v_cndmask_b32_e32 v94, v229, v3, vcc
	v_or_b32_e32 v3, 0x6b0, v81
	v_sub_u32_e32 v3, v80, v3
	v_cmp_lt_i32_e32 vcc, -1, v3
	v_cvt_f32_u32_e32 v3, v3
	v_fma_f32 v3, -v124, v3, v9
	v_cndmask_b32_e32 v95, v229, v3, vcc
	v_or_b32_e32 v3, 0x700, v81
	v_sub_u32_e32 v3, v80, v3
	v_cmp_lt_i32_e32 vcc, -1, v3
	v_cvt_f32_u32_e32 v3, v3
	v_max3_f32 v2, v2, v94, v95
	v_fma_f32 v3, -v124, v3, v10
	v_cndmask_b32_e32 v96, v229, v3, vcc
	v_or_b32_e32 v3, 0x710, v81
	v_sub_u32_e32 v3, v80, v3
	v_cmp_lt_i32_e32 vcc, -1, v3
	v_cvt_f32_u32_e32 v3, v3
	v_fma_f32 v3, -v124, v3, v11
	v_cndmask_b32_e32 v97, v229, v3, vcc
	v_or_b32_e32 v3, 0x720, v81
	v_sub_u32_e32 v3, v80, v3
	v_cmp_lt_i32_e32 vcc, -1, v3
	v_cvt_f32_u32_e32 v3, v3
	v_max3_f32 v2, v2, v96, v97
	v_fma_f32 v3, -v124, v3, v12
	v_cndmask_b32_e32 v114, v229, v3, vcc
	v_or_b32_e32 v3, 0x730, v81
	v_sub_u32_e32 v3, v80, v3
	v_cmp_lt_i32_e32 vcc, -1, v3
	v_cvt_f32_u32_e32 v3, v3
	v_fma_f32 v3, -v124, v3, v13
	v_cndmask_b32_e32 v115, v229, v3, vcc
	v_or_b32_e32 v3, 0x780, v81
	v_sub_u32_e32 v3, v80, v3
	v_cmp_lt_i32_e32 vcc, -1, v3
	v_cvt_f32_u32_e32 v3, v3
	v_max3_f32 v2, v2, v114, v115
	v_fma_f32 v3, -v124, v3, v14
	v_cndmask_b32_e32 v116, v229, v3, vcc
	v_or_b32_e32 v3, 0x790, v81
	v_sub_u32_e32 v3, v80, v3
	v_cmp_lt_i32_e32 vcc, -1, v3
	v_cvt_f32_u32_e32 v3, v3
	v_fma_f32 v3, -v124, v3, v15
	v_cndmask_b32_e32 v117, v229, v3, vcc
	v_or_b32_e32 v3, 0x7a0, v81
	v_sub_u32_e32 v3, v80, v3
	v_cmp_lt_i32_e32 vcc, -1, v3
	v_cvt_f32_u32_e32 v3, v3
	v_max3_f32 v2, v2, v116, v117
	v_fma_f32 v3, -v124, v3, v16
	v_cndmask_b32_e32 v125, v229, v3, vcc
	v_or_b32_e32 v3, 0x7b0, v81
	v_sub_u32_e32 v3, v80, v3
	v_cmp_lt_i32_e32 vcc, -1, v3
	v_cvt_f32_u32_e32 v3, v3
	s_and_b64 vcc, s[0:1], vcc
	v_add_u32_e32 v80, 64, v4
	v_fma_f32 v3, -v124, v3, v17
	v_cndmask_b32_e32 v81, v229, v3, vcc
	v_xor_b32_e32 v3, 32, v228
	v_cmp_lt_i32_e32 vcc, v3, v80
	v_max3_f32 v2, v2, v125, v81
	s_nop 0
	v_cndmask_b32_e32 v3, v228, v3, vcc
	v_lshlrev_b32_e32 v172, 2, v3
	ds_bpermute_b32 v3, v172, v2
	s_waitcnt lgkmcnt(0)
	v_max_f32_e32 v3, v3, v3
	v_max_f32_e32 v2, v2, v3
	v_cmp_neq_f32_e32 vcc, s5, v2
	s_nop 1
	v_cndmask_b32_e32 v126, 0, v2, vcc
	v_sub_f32_e32 v4, v52, v126
	v_sub_f32_e32 v52, v88, v126
	v_sub_f32_e32 v22, v38, v126
	v_sub_f32_e32 v38, v44, v126
	v_sub_f32_e32 v44, v82, v126
	v_exp_f32_e32 v82, v52
	v_sub_f32_e32 v52, v89, v126
	v_sub_f32_e32 v23, v39, v126
	v_sub_f32_e32 v39, v45, v126
	v_sub_f32_e32 v45, v83, v126
	v_exp_f32_e32 v83, v52
	v_sub_f32_e32 v52, v90, v126
	v_sub_f32_e32 v18, v34, v126
	v_sub_f32_e32 v34, v40, v126
	v_sub_f32_e32 v40, v46, v126
	v_sub_f32_e32 v46, v84, v126
	v_exp_f32_e32 v84, v52
	v_sub_f32_e32 v52, v91, v126
	v_sub_f32_e32 v19, v35, v126
	v_sub_f32_e32 v35, v41, v126
	v_sub_f32_e32 v41, v47, v126
	v_sub_f32_e32 v47, v85, v126
	v_exp_f32_e32 v85, v52
	v_sub_f32_e32 v52, v92, v126
	v_sub_f32_e32 v20, v36, v126
	v_sub_f32_e32 v36, v42, v126
	v_sub_f32_e32 v42, v48, v126
	v_sub_f32_e32 v48, v86, v126
	v_exp_f32_e32 v86, v52
	v_sub_f32_e32 v52, v93, v126
	v_sub_f32_e32 v21, v37, v126
	v_sub_f32_e32 v37, v43, v126
	v_sub_f32_e32 v43, v49, v126
	v_sub_f32_e32 v49, v87, v126
	v_exp_f32_e32 v87, v52
	v_sub_f32_e32 v52, v94, v126
	v_exp_f32_e32 v88, v52
	v_sub_f32_e32 v52, v95, v126
	v_exp_f32_e32 v89, v52
	v_sub_f32_e32 v52, v96, v126
	v_exp_f32_e32 v90, v52
	v_sub_f32_e32 v52, v97, v126
	v_exp_f32_e32 v91, v52
	v_sub_f32_e32 v52, v114, v126
	v_sub_f32_e32 v2, v66, v126
	v_exp_f32_e32 v92, v52
	v_sub_f32_e32 v52, v115, v126
	v_exp_f32_e32 v2, v2
	v_sub_f32_e32 v3, v67, v126
	v_exp_f32_e32 v93, v52
	v_sub_f32_e32 v52, v116, v126
	v_exp_f32_e32 v3, v3
	v_exp_f32_e32 v94, v52
	v_sub_f32_e32 v52, v117, v126
	v_exp_f32_e32 v4, v4
	v_sub_f32_e32 v5, v53, v126
	v_exp_f32_e32 v95, v52
	v_sub_f32_e32 v52, v125, v126
	v_exp_f32_e32 v5, v5
	v_sub_f32_e32 v6, v54, v126
	v_exp_f32_e32 v96, v52
	v_sub_f32_e32 v52, v81, v126
	v_exp_f32_e32 v6, v6
	v_sub_f32_e32 v7, v55, v126
	v_exp_f32_e32 v97, v52
	v_add_f32_e32 v52, 0, v2
	v_exp_f32_e32 v7, v7
	v_sub_f32_e32 v8, v56, v126
	v_add_f32_e32 v52, v3, v52
	v_exp_f32_e32 v8, v8
	v_sub_f32_e32 v9, v57, v126
	v_add_f32_e32 v52, v4, v52
	v_exp_f32_e32 v9, v9
	v_sub_f32_e32 v10, v58, v126
	v_add_f32_e32 v52, v5, v52
	v_exp_f32_e32 v10, v10
	v_sub_f32_e32 v11, v59, v126
	v_add_f32_e32 v52, v6, v52
	v_exp_f32_e32 v11, v11
	v_sub_f32_e32 v12, v60, v126
	v_add_f32_e32 v52, v7, v52
	v_exp_f32_e32 v12, v12
	v_sub_f32_e32 v13, v61, v126
	v_add_f32_e32 v52, v8, v52
	v_exp_f32_e32 v13, v13
	v_sub_f32_e32 v14, v62, v126
	v_add_f32_e32 v52, v9, v52
	v_exp_f32_e32 v14, v14
	v_sub_f32_e32 v15, v63, v126
	v_add_f32_e32 v52, v10, v52
	v_exp_f32_e32 v15, v15
	v_sub_f32_e32 v16, v64, v126
	v_add_f32_e32 v52, v11, v52
	v_exp_f32_e32 v16, v16
	v_sub_f32_e32 v17, v65, v126
	v_add_f32_e32 v52, v12, v52
	v_exp_f32_e32 v17, v17
	v_add_f32_e32 v52, v13, v52
	v_exp_f32_e32 v18, v18
	v_add_f32_e32 v52, v14, v52
	v_exp_f32_e32 v19, v19
	v_add_f32_e32 v52, v15, v52
	v_exp_f32_e32 v20, v20
	v_add_f32_e32 v52, v16, v52
; __device__ __forceinline__ void unit(LAS unsigned char* lds, const bf16* Z, const bf16* kct, const bf16* vct, bf16* OAp, int b, int g, int iq, const int tid_in) {
;     ...
;             for (int r = 0; r < 16; ++r) { const float e = __builtin_amdgcn_exp2f(p[blk][r] - msafe); p[blk][r] = e; l += e; }
;         l += __shfl_xor(l, 32);
;         const float inv = l > 0.f ? 1.0f / l : 0.f;
; #pragma unroll
;         for (int blk = 0; blk < 4; ++blk)
; #pragma unroll
;             for (int r = 0; r < 16; ++r) p[blk][r] *= inv;
; #pragma unroll
;         for (int blk = 0; blk < 4; ++blk)
; #pragma unroll
;             for (int rq = 0; rq < 4; ++rq) { const int n = 8 * blk + 2 * rq + hi;
;                 IA[(j * 64 + tl) * 32 + n] = 2.f * (p[blk][4 * rq] + p[blk][4 * rq + 1] + p[blk][4 * rq + 2]) + p[blk][4 * rq + 3];
;                 IB[(j * 64 + tl) * 32 + n] = p[blk][4 * rq + 3]; }
	v_exp_f32_e32 v21, v21
	v_add_f32_e32 v52, v17, v52
	v_exp_f32_e32 v22, v22
	v_add_f32_e32 v52, v18, v52
	v_exp_f32_e32 v23, v23
	v_add_f32_e32 v52, v19, v52
	v_exp_f32_e32 v34, v34
	v_add_f32_e32 v52, v20, v52
	v_exp_f32_e32 v35, v35
	v_add_f32_e32 v52, v21, v52
	v_exp_f32_e32 v36, v36
	v_add_f32_e32 v52, v22, v52
	v_exp_f32_e32 v37, v37
	v_add_f32_e32 v52, v23, v52
	v_exp_f32_e32 v38, v38
	v_add_f32_e32 v52, v34, v52
	v_exp_f32_e32 v39, v39
	v_add_f32_e32 v52, v35, v52
	v_exp_f32_e32 v40, v40
	v_add_f32_e32 v52, v36, v52
	v_exp_f32_e32 v41, v41
	v_add_f32_e32 v52, v37, v52
	v_exp_f32_e32 v42, v42
	v_add_f32_e32 v52, v38, v52
	v_exp_f32_e32 v43, v43
	v_add_f32_e32 v52, v39, v52
	v_exp_f32_e32 v44, v44
	v_add_f32_e32 v52, v40, v52
	v_exp_f32_e32 v45, v45
	v_add_f32_e32 v52, v41, v52
	v_exp_f32_e32 v46, v46
	v_add_f32_e32 v52, v42, v52
	v_exp_f32_e32 v47, v47
	v_add_f32_e32 v52, v43, v52
	v_exp_f32_e32 v48, v48
	v_add_f32_e32 v52, v44, v52
	v_exp_f32_e32 v49, v49
	v_sub_f32_e32 v24, v24, v126
	v_add_f32_e32 v52, v45, v52
	v_exp_f32_e32 v24, v24
	v_sub_f32_e32 v25, v25, v126
	v_add_f32_e32 v52, v46, v52
	v_exp_f32_e32 v25, v25
	v_sub_f32_e32 v26, v26, v126
	v_add_f32_e32 v52, v47, v52
	v_exp_f32_e32 v26, v26
	v_sub_f32_e32 v27, v27, v126
	v_add_f32_e32 v52, v48, v52
	v_exp_f32_e32 v27, v27
	v_sub_f32_e32 v28, v28, v126
	v_add_f32_e32 v52, v49, v52
	v_exp_f32_e32 v28, v28
	v_sub_f32_e32 v29, v29, v126
	v_add_f32_e32 v52, v24, v52
	v_exp_f32_e32 v29, v29
	v_sub_f32_e32 v30, v30, v126
	v_add_f32_e32 v52, v25, v52
	v_exp_f32_e32 v30, v30
	v_sub_f32_e32 v31, v31, v126
	v_add_f32_e32 v52, v26, v52
	v_exp_f32_e32 v31, v31
	v_sub_f32_e32 v32, v32, v126
	v_add_f32_e32 v52, v27, v52
	v_exp_f32_e32 v32, v32
	v_sub_f32_e32 v33, v33, v126
	v_add_f32_e32 v52, v28, v52
	v_exp_f32_e32 v33, v33
	v_add_f32_e32 v52, v29, v52
	v_add_f32_e32 v52, v30, v52
	v_add_f32_e32 v52, v31, v52
	v_add_f32_e32 v52, v32, v52
	v_add_f32_e32 v52, v33, v52
	v_add_f32_e32 v52, v82, v52
	v_add_f32_e32 v52, v83, v52
	v_add_f32_e32 v52, v84, v52
	v_add_f32_e32 v52, v85, v52
	v_add_f32_e32 v52, v86, v52
	v_add_f32_e32 v52, v87, v52
	v_add_f32_e32 v52, v88, v52
	v_add_f32_e32 v52, v89, v52
	v_add_f32_e32 v52, v90, v52
	v_add_f32_e32 v52, v91, v52
	v_add_f32_e32 v52, v92, v52
	v_add_f32_e32 v52, v93, v52
	v_add_f32_e32 v52, v94, v52
	v_add_f32_e32 v52, v95, v52
	v_add_f32_e32 v52, v96, v52
	v_add_f32_e32 v52, v97, v52
	ds_bpermute_b32 v53, v172, v52
	s_waitcnt lgkmcnt(0)
	v_add_f32_e32 v52, v52, v53
	v_div_scale_f32 v53, s[6:7], v52, v52, 1.0
	v_rcp_f32_e32 v54, v53
	v_cmp_lt_f32_e64 s[0:1], 0, v52
	v_fma_f32 v55, -v53, v54, 1.0
	v_fmac_f32_e32 v54, v55, v54
	v_div_scale_f32 v55, vcc, 1.0, v52, 1.0
	v_mul_f32_e32 v56, v55, v54
	v_fma_f32 v57, -v53, v56, v55
	v_fmac_f32_e32 v56, v57, v54
	v_fma_f32 v53, -v53, v56, v55
	v_div_fmas_f32 v53, v53, v54, v56
	v_div_fixup_f32 v52, v53, v52, 1.0
	v_cndmask_b32_e64 v114, 0, v52, s[0:1]
	v_pk_mul_f32 v[2:3], v[2:3], v[114:115] op_sel_hi:[1,0]
	v_pk_mul_f32 v[6:7], v[6:7], v[114:115] op_sel_hi:[1,0]
	v_pk_mul_f32 v[116:117], v[10:11], v[114:115] op_sel_hi:[1,0]
	s_lshl_b32 s0, s4, 11
	v_lshlrev_b32_e32 v10, 5, v68
	v_pk_mul_f32 v[4:5], v[4:5], v[114:115] op_sel_hi:[1,0]
	v_pk_mul_f32 v[8:9], v[8:9], v[114:115] op_sel_hi:[1,0]
	v_pk_mul_f32 v[126:127], v[12:13], v[114:115] op_sel_hi:[1,0]
	v_or3_b32 v10, v10, s0, v74
	v_lshlrev_b32_e32 v216, 5, v68
	v_or_b32_e32 v216, s0, v216
	v_lshl_add_u32 v216, v216, 2, 0
	v_add_u32_e32 v216, 0xd400, v216
	v_and_b32_e32 v217, 31, v68
	v_add_lshl_u32 v217, v217, v74, 2
	v_mov_b32_e32 v218, 0x7c
	v_add_f32_e32 v11, v2, v3
	v_add_f32_e32 v13, v6, v7
	v_add_f32_e32 v11, v4, v11
	v_lshl_add_u32 v10, v10, 2, 0
	v_add_f32_e32 v13, v8, v13
	v_pk_mul_f32 v[128:129], v[14:15], v[114:115] op_sel_hi:[1,0]
	v_fma_f32 v11, 2.0, v11, v5
	v_add_u32_e32 v12, 0x15400, v10
	v_fma_f32 v13, 2.0, v13, v9
	v_add_u32_e32 v10, 0xd400, v10
	v_pk_mul_f32 v[130:131], v[16:17], v[114:115] op_sel_hi:[1,0]
	v_add_u32_e32 v219, 0, v217
	v_add_u32_e32 v220, 8, v217
	v_and_or_b32 v219, v219, v218, v216
	v_and_or_b32 v220, v220, v218, v216
	ds_write_b32 v219, v11
	ds_write_b32 v219, v5 offset:32768
	ds_write_b32 v220, v13
	ds_write_b32 v220, v9 offset:32768
	v_add_f32_e32 v11, v116, v117
	v_add_f32_e32 v13, v128, v129
	v_add_f32_e32 v11, v126, v11
	v_add_f32_e32 v13, v130, v13
	v_pk_mul_f32 v[132:133], v[18:19], v[114:115] op_sel_hi:[1,0]
	v_pk_mul_f32 v[136:137], v[22:23], v[114:115] op_sel_hi:[1,0]
	v_fma_f32 v11, 2.0, v11, v127
	v_fma_f32 v13, 2.0, v13, v131
	v_pk_mul_f32 v[134:135], v[20:21], v[114:115] op_sel_hi:[1,0]
	v_pk_mul_f32 v[138:139], v[34:35], v[114:115] op_sel_hi:[1,0]
	v_add_u32_e32 v219, 16, v217
	v_add_u32_e32 v220, 24, v217
	v_and_or_b32 v219, v219, v218, v216
	v_and_or_b32 v220, v220, v218, v216
	ds_write_b32 v219, v11
	ds_write_b32 v219, v127 offset:32768
	ds_write_b32 v220, v13
	ds_write_b32 v220, v131 offset:32768
	v_add_f32_e32 v11, v132, v133
	v_add_f32_e32 v13, v136, v137
	v_add_f32_e32 v11, v134, v11
	v_add_f32_e32 v13, v138, v13
	v_pk_mul_f32 v[140:141], v[36:37], v[114:115] op_sel_hi:[1,0]
	v_pk_mul_f32 v[144:145], v[40:41], v[114:115] op_sel_hi:[1,0]
	v_fma_f32 v11, 2.0, v11, v135
	v_fma_f32 v13, 2.0, v13, v139
	v_pk_mul_f32 v[142:143], v[38:39], v[114:115] op_sel_hi:[1,0]
	v_pk_mul_f32 v[146:147], v[42:43], v[114:115] op_sel_hi:[1,0]
	v_add_u32_e32 v219, 32, v217
	v_add_u32_e32 v220, 40, v217
	v_and_or_b32 v219, v219, v218, v216
	v_and_or_b32 v220, v220, v218, v216
	ds_write_b32 v219, v11
	ds_write_b32 v219, v135 offset:32768
	ds_write_b32 v220, v13
	ds_write_b32 v220, v139 offset:32768
	v_add_f32_e32 v11, v140, v141
; #define LAS __attribute__((address_space(3)))
; __device__ __forceinline__ unsigned cvt_pk_bf16(float lo, float hi) { f32x2_t v = {lo, hi}; bf16x2_t b = __builtin_convertvector(v, bf16x2_t); return __builtin_bit_cast(unsigned, b); }
; #define MFMA32(a, b, c) __builtin_amdgcn_mfma_f32_32x32x16_bf16((a), (b), (c), 0, 0, 0)
; __device__ __forceinline__ void unit(LAS unsigned char* lds, const bf16* Z, const bf16* kct, const bf16* vct, bf16* OAp, int b, int g, int iq, const int tid_in) {
;     ...
;                 IA[(j * 64 + tl) * 32 + n] = 2.f * (p[blk][4 * rq] + p[blk][4 * rq + 1] + p[blk][4 * rq + 2]) + p[blk][4 * rq + 3];
;                 IB[(j * 64 + tl) * 32 + n] = p[blk][4 * rq + 3]; }
;         f32x16 oc[2];
; #pragma unroll
;         for (int r = 0; r < 16; ++r) { oc[0][r] = 0.f; oc[1][r] = 0.f; }
; #pragma unroll
;         for (int s = 0; s < 8; ++s) { const int blk = s >> 1, rb = 8 * (s & 1);
;             u32x4 pw; pw.x = cvt_pk_bf16(p[blk][rb + 0], p[blk][rb + 1]); pw.y = cvt_pk_bf16(p[blk][rb + 2], p[blk][rb + 3]); pw.z = cvt_pk_bf16(p[blk][rb + 4], p[blk][rb + 5]); pw.w = cvt_pk_bf16(p[blk][rb + 6], p[blk][rb + 7]);
;             const bf16x8 pa = __builtin_bit_cast(bf16x8, pw);
; #pragma unroll
;             for (int db = 0; db < 2; ++db) { const bf16x8 vf = *(const LAS bf16x8*)(VC + (32 * db + r32) * VST2 + 16 * s + 8 * hi); oc[db] = MFMA32(vf, pa, oc[db]); } }
; #pragma unroll
;         for (int r = 0; r < 16; ++r) { otot[0][r] += gate[0] * oc[0][r]; otot[1][r] += gate[0] * oc[1][r]; }
;     }
;     __syncthreads();
;     {
;         const int n = lane & 31;
; #pragma unroll
;         for (int q = 0; q < 4; ++q) { const int tk = (tid >> 5) + 16 * q;
;             float imp = 0.f;
; #pragma unroll
;             for (int jj = 0; jj < 4; ++jj) { imp += IA[(jj * 64 + tk) * 32 + n]; if (n > 0) imp += IB[(jj * 64 + tk) * 32 + n - 1]; }
;             const bool valid = n <= iq, forced = (n == 0) || (n == iq) || (n == iq - 1);
;             const float sc = forced ? 1e4f : (valid ? imp : -1.0f);
;             int cnt = 0;
; #pragma unroll
;             for (int mm = 0; mm < 32; ++mm) { const float so = __shfl(sc, (lane & 32) + mm); cnt += (so > sc || (so == sc && mm < n)) ? 1 : 0; }
;             const unsigned long long bal = __ballot(cnt < 16);
;             if (n == 0) MSK[tk] = (unsigned)((lane & 32) ? (bal >> 32) : bal); }
	v_add_f32_e32 v13, v144, v145
	v_add_f32_e32 v11, v142, v11
	v_add_f32_e32 v13, v146, v13
	v_pk_mul_f32 v[60:61], v[44:45], v[114:115] op_sel_hi:[1,0]
	v_pk_mul_f32 v[64:65], v[48:49], v[114:115] op_sel_hi:[1,0]
	v_fma_f32 v11, 2.0, v11, v143
	v_fma_f32 v13, 2.0, v13, v147
	v_pk_mul_f32 v[62:63], v[46:47], v[114:115] op_sel_hi:[1,0]
	v_pk_mul_f32 v[66:67], v[24:25], v[114:115] op_sel_hi:[1,0]
	v_add_u32_e32 v219, 48, v217
	v_add_u32_e32 v220, 56, v217
	v_and_or_b32 v219, v219, v218, v216
	v_and_or_b32 v220, v220, v218, v216
	ds_write_b32 v219, v11
	ds_write_b32 v219, v143 offset:32768
	ds_write_b32 v220, v13
	ds_write_b32 v220, v147 offset:32768
	v_add_f32_e32 v11, v60, v61
	v_add_f32_e32 v13, v64, v65
	v_add_f32_e32 v11, v62, v11
	v_add_f32_e32 v13, v66, v13
	v_pk_mul_f32 v[52:53], v[26:27], v[114:115] op_sel_hi:[1,0]
	v_pk_mul_f32 v[56:57], v[30:31], v[114:115] op_sel_hi:[1,0]
	v_fma_f32 v11, 2.0, v11, v63
	v_fma_f32 v13, 2.0, v13, v67
	v_pk_mul_f32 v[54:55], v[28:29], v[114:115] op_sel_hi:[1,0]
	v_pk_mul_f32 v[58:59], v[32:33], v[114:115] op_sel_hi:[1,0]
	v_add_u32_e32 v219, 64, v217
	v_add_u32_e32 v220, 72, v217
	v_and_or_b32 v219, v219, v218, v216
	v_and_or_b32 v220, v220, v218, v216
	ds_write_b32 v219, v11
	ds_write_b32 v219, v63 offset:32768
	ds_write_b32 v220, v13
	ds_write_b32 v220, v67 offset:32768
	v_add_f32_e32 v11, v52, v53
	v_add_f32_e32 v13, v56, v57
	v_add_f32_e32 v11, v54, v11
	v_add_f32_e32 v13, v58, v13
	v_pk_mul_f32 v[42:43], v[82:83], v[114:115] op_sel_hi:[1,0]
	v_pk_mul_f32 v[46:47], v[86:87], v[114:115] op_sel_hi:[1,0]
	v_fma_f32 v11, 2.0, v11, v55
	v_fma_f32 v13, 2.0, v13, v59
	v_pk_mul_f32 v[44:45], v[84:85], v[114:115] op_sel_hi:[1,0]
	v_pk_mul_f32 v[48:49], v[88:89], v[114:115] op_sel_hi:[1,0]
	v_add_u32_e32 v219, 80, v217
	v_add_u32_e32 v220, 88, v217
	v_and_or_b32 v219, v219, v218, v216
	v_and_or_b32 v220, v220, v218, v216
	ds_write_b32 v219, v11
	ds_write_b32 v219, v55 offset:32768
	ds_write_b32 v220, v13
	ds_write_b32 v220, v59 offset:32768
	v_add_f32_e32 v11, v42, v43
	v_add_f32_e32 v13, v46, v47
	v_add_f32_e32 v11, v44, v11
	v_add_f32_e32 v13, v48, v13
	v_pk_mul_f32 v[34:35], v[90:91], v[114:115] op_sel_hi:[1,0]
	v_pk_mul_f32 v[38:39], v[94:95], v[114:115] op_sel_hi:[1,0]
	v_fma_f32 v11, 2.0, v11, v45
	v_fma_f32 v13, 2.0, v13, v49
	v_pk_mul_f32 v[36:37], v[92:93], v[114:115] op_sel_hi:[1,0]
	v_pk_mul_f32 v[40:41], v[96:97], v[114:115] op_sel_hi:[1,0]
	v_add_u32_e32 v219, 96, v217
	v_add_u32_e32 v220, 104, v217
	v_and_or_b32 v219, v219, v218, v216
	v_and_or_b32 v220, v220, v218, v216
	ds_write_b32 v219, v11
	ds_write_b32 v219, v45 offset:32768
	ds_write_b32 v220, v13
	ds_write_b32 v220, v49 offset:32768
	v_add_f32_e32 v11, v34, v35
	v_add_f32_e32 v13, v38, v39
	v_add_f32_e32 v11, v36, v11
	v_add_f32_e32 v13, v40, v13
	v_fma_f32 v11, 2.0, v11, v37
	v_fma_f32 v13, 2.0, v13, v41
	s_movk_i32 s0, 0x110
	v_add_u32_e32 v219, 112, v217
	v_add_u32_e32 v220, 120, v217
	v_and_or_b32 v219, v219, v218, v216
	v_and_or_b32 v220, v220, v218, v216
	ds_write_b32 v219, v11
	ds_write_b32 v219, v37 offset:32768
	ds_write_b32 v220, v13
	ds_write_b32 v220, v41 offset:32768
	v_mad_u32_u24 v81, v73, s0, v76
	v_cvt_pk_bf16_f32 v2, v2, v3
	v_cvt_pk_bf16_f32 v3, v4, v5
	v_cvt_pk_bf16_f32 v4, v6, v7
	v_cvt_pk_bf16_f32 v5, v8, v9
	ds_read_b128 v[6:9], v81 offset:36864
	ds_read_b128 v[82:85], v81 offset:36896
	s_waitcnt lgkmcnt(1)
	v_mfma_f32_32x32x16_bf16 v[18:33], v[6:9], v[2:5], 0
	ds_read_b128 v[6:9], v81 offset:45568
	v_cvt_pk_bf16_f32 v86, v116, v117
	v_cvt_pk_bf16_f32 v87, v126, v127
	v_cvt_pk_bf16_f32 v88, v128, v129
	v_cvt_pk_bf16_f32 v89, v130, v131
	v_cvt_pk_bf16_f32 v60, v60, v61
	v_cvt_pk_bf16_f32 v61, v62, v63
	s_waitcnt lgkmcnt(1)
	v_mfma_f32_32x32x16_bf16 v[18:33], v[82:85], v[86:89], v[18:33]
	ds_read_b128 v[82:85], v81 offset:45600
	v_cvt_pk_bf16_f32 v62, v64, v65
	v_cvt_pk_bf16_f32 v63, v66, v67
	ds_read_b128 v[64:67], v81 offset:36992
	v_cvt_pk_bf16_f32 v52, v52, v53
	v_cvt_pk_bf16_f32 v53, v54, v55
	v_cvt_pk_bf16_f32 v54, v56, v57
	s_waitcnt lgkmcnt(2)
	v_mfma_f32_32x32x16_bf16 v[2:17], v[6:9], v[2:5], 0
	v_cvt_pk_bf16_f32 v55, v58, v59
	ds_read_b128 v[56:59], v81 offset:37024
	v_cvt_pk_bf16_f32 v42, v42, v43
	v_cvt_pk_bf16_f32 v43, v44, v45
	v_cvt_pk_bf16_f32 v44, v46, v47
	v_cvt_pk_bf16_f32 v45, v48, v49
	ds_read_b128 v[46:49], v81 offset:37056
	s_waitcnt lgkmcnt(3)
	v_mfma_f32_32x32x16_bf16 v[2:17], v[82:85], v[86:89], v[2:17]
	ds_read_b128 v[86:89], v81 offset:36928
	v_cvt_pk_bf16_f32 v82, v132, v133
	v_cvt_pk_bf16_f32 v83, v134, v135
	v_cvt_pk_bf16_f32 v84, v136, v137
	v_cvt_pk_bf16_f32 v85, v138, v139
	v_cvt_pk_bf16_f32 v34, v34, v35
	v_cvt_pk_bf16_f32 v35, v36, v37
	s_waitcnt lgkmcnt(0)
	v_mfma_f32_32x32x16_bf16 v[18:33], v[86:89], v[82:85], v[18:33]
	ds_read_b128 v[86:89], v81 offset:45632
	v_cvt_pk_bf16_f32 v36, v38, v39
	v_cvt_pk_bf16_f32 v37, v40, v41
	ds_read_b128 v[38:41], v81 offset:37088
	v_cmp_ne_u32_e64 s[0:1], 0, v73
	s_waitcnt lgkmcnt(1)
	v_mfma_f32_32x32x16_bf16 v[2:17], v[86:89], v[82:85], v[2:17]
	ds_read_b128 v[86:89], v81 offset:36960
	v_cvt_pk_bf16_f32 v82, v140, v141
	v_cvt_pk_bf16_f32 v83, v142, v143
	v_cvt_pk_bf16_f32 v84, v144, v145
	v_cvt_pk_bf16_f32 v85, v146, v147
	s_waitcnt lgkmcnt(0)
	s_nop 0
	v_mfma_f32_32x32x16_bf16 v[18:33], v[86:89], v[82:85], v[18:33]
	ds_read_b128 v[86:89], v81 offset:45664
	v_mfma_f32_32x32x16_bf16 v[18:33], v[64:67], v[60:63], v[18:33]
	ds_read_b128 v[64:67], v81 offset:45696
	s_waitcnt lgkmcnt(1)
	v_mfma_f32_32x32x16_bf16 v[2:17], v[86:89], v[82:85], v[2:17]
	v_mfma_f32_32x32x16_bf16 v[18:33], v[56:59], v[52:55], v[18:33]
	ds_read_b128 v[56:59], v81 offset:45728
	s_waitcnt lgkmcnt(1)
	v_mfma_f32_32x32x16_bf16 v[2:17], v[64:67], v[60:63], v[2:17]
	v_mfma_f32_32x32x16_bf16 v[18:33], v[46:49], v[42:45], v[18:33]
	ds_read_b128 v[46:49], v81 offset:45760
	s_waitcnt lgkmcnt(1)
	v_mfma_f32_32x32x16_bf16 v[2:17], v[56:59], v[52:55], v[2:17]
	v_mfma_f32_32x32x16_bf16 v[18:33], v[38:41], v[34:37], v[18:33]
	ds_read_b128 v[38:41], v81 offset:45792
	s_waitcnt lgkmcnt(0)
	s_barrier
	v_mfma_f32_32x32x16_bf16 v[2:17], v[46:49], v[42:45], v[2:17]
	v_mfma_f32_32x32x16_bf16 v[2:17], v[38:41], v[34:37], v[2:17]
	s_cmp_lt_u32 s18, 16
	s_cbranch_scc0 .Lnsa_sel_rank
	s_add_i32 s19, s18, -1
	v_lshlrev_b32_e32 v36, 2, v78
	v_cmp_gt_u32_e32 vcc, 64, v78
	s_and_saveexec_b64 s[0:1], vcc
	v_add_u32_e32 v35, 0x1d400, v36
	v_mov_b32_e32 v34, 0xffff
	ds_write_b32 v35, v34
	s_branch .Lnsa_sel_join
.Lnsa_sel_rank:
	v_lshrrev_b32_e32 v216, 5, v78
	v_add_u32_e32 v217, v216, v73
	v_add_u32_e32 v218, -1, v217
	v_and_b32_e32 v217, 31, v217
	v_and_b32_e32 v218, 31, v218
	v_lshl_or_b32 v217, v216, 5, v217
	v_lshl_or_b32 v218, v216, 5, v218
	v_lshl_add_u32 v34, v217, 2, 0
	ds_read_b32 v35, v34 offset:54272
	v_lshlrev_b32_e32 v36, 2, v78
	s_waitcnt lgkmcnt(0)
	v_add_f32_e32 v35, 0, v35
	s_and_saveexec_b64 s[4:5], s[0:1]
	s_cbranch_execz .LBB0_418
	s_add_i32 s6, 0, 0x15400
	v_lshl_add_u32 v37, v218, 2, s6
	ds_read_b32 v37, v37
	s_waitcnt lgkmcnt(0)
	v_add_f32_e32 v35, v35, v37

; __device__ __forceinline__ void unit(LAS unsigned char* lds, const bf16* Z, const bf16* kct, const bf16* vct, bf16* OAp, int b, int g, int iq, const int tid_in) {
;     ...
;     __syncthreads();
;     const unsigned mymask = MSK[tl];
;     if (tid < 64) {
;         unsigned un = MSK[lane];
; #pragma unroll
;         for (int o = 1; o < 64; o <<= 1) un |= __shfl_xor(un, o);
;         if (lane == 0) { int cnt = 0;
;             for (int n = iq; n >= 0; --n) if ((un >> n) & 1u) TL[1 + cnt++] = n | 0x100;
;             for (int n = iq; n >= (iq >= 8 ? iq - 8 : 0); --n) TL[1 + cnt++] = n | 0x200;
;             TL[0] = cnt; }
.Lnsa_sel_join:
	s_or_b64 exec, exec, s[0:1]
	v_lshl_add_u32 v34, v68, 2, 0
	v_add_u32_e32 v34, 0x1d400, v34
	s_waitcnt lgkmcnt(0)
	s_barrier
	ds_read_b32 v173, v34
	v_cmp_gt_i32_e32 vcc, 64, v78
	s_and_saveexec_b64 s[0:1], vcc
	s_cbranch_execz .LBB0_470
	v_lshl_add_u32 v34, v79, 2, 0
	v_add_u32_e32 v34, 0x1d400, v34
	ds_read_b32 v34, v34
	v_xor_b32_e32 v35, 1, v228
	v_cmp_lt_i32_e32 vcc, v35, v80
	s_nop 1
	v_cndmask_b32_e32 v35, v228, v35, vcc
	v_lshlrev_b32_e32 v35, 2, v35
	s_waitcnt lgkmcnt(0)
	ds_bpermute_b32 v35, v35, v34
	s_waitcnt lgkmcnt(0)
	v_or_b32_e32 v34, v35, v34
	v_xor_b32_e32 v35, 2, v228
	v_cmp_lt_i32_e32 vcc, v35, v80
	s_nop 1
	v_cndmask_b32_e32 v35, v228, v35, vcc
	v_lshlrev_b32_e32 v35, 2, v35
	ds_bpermute_b32 v35, v35, v34
	s_waitcnt lgkmcnt(0)
	v_or_b32_e32 v34, v35, v34
	v_xor_b32_e32 v35, 4, v228
	v_cmp_lt_i32_e32 vcc, v35, v80
	s_nop 1
	v_cndmask_b32_e32 v35, v228, v35, vcc
	v_lshlrev_b32_e32 v35, 2, v35
	ds_bpermute_b32 v35, v35, v34
	s_waitcnt lgkmcnt(0)
	v_or_b32_e32 v34, v35, v34
	v_xor_b32_e32 v35, 8, v228
	v_cmp_lt_i32_e32 vcc, v35, v80
	s_nop 1
	v_cndmask_b32_e32 v35, v228, v35, vcc
	v_lshlrev_b32_e32 v35, 2, v35
	ds_bpermute_b32 v35, v35, v34
	s_waitcnt lgkmcnt(0)
	v_or_b32_e32 v34, v35, v34
	v_xor_b32_e32 v35, 16, v228
	v_cmp_lt_i32_e32 vcc, v35, v80
	s_nop 1
	v_cndmask_b32_e32 v35, v228, v35, vcc
	v_lshlrev_b32_e32 v35, 2, v35
	ds_bpermute_b32 v35, v35, v34
	v_cmp_eq_u32_e32 vcc, 0, v79
	s_waitcnt lgkmcnt(0)
	v_or_b32_e32 v34, v35, v34
	ds_bpermute_b32 v35, v172, v34
	s_and_b64 exec, exec, vcc
	s_cbranch_execz .LBB0_470
	s_waitcnt lgkmcnt(0)
	v_or_b32_e32 v35, v35, v34
	v_mov_b32_e32 v34, 0
	s_mov_b32 s6, s18
	s_branch .LBB0_460
